# attention: expert-weight conversion consumer moved from mid-iteration to end of iteration (loads in flight a whole iteration), both layers
# baseline (speedup 1.0000x reference)
; DEVI f32x4 ld_nt(const float* p) { return __builtin_nontemporal_load((const f32x4*)p); }
; DEVI CvSlice cv_slice(const Params& p, int l, int s, int lane) {
;     CvSlice c;
;     if (s < NS_W13) {
;         const int e = s >> 9, r = s & 511, hb = r & 7, mat = (r >> 3) & 1, ks = r >> 4;
;         const float* W = mat ? (e < NE ? p.w3 + ((size_t)l * NE + e) * 1024 * 256 : p.ws3 + (size_t)l * 1024 * 256)
;                              : (e < NE ? p.w1 + ((size_t)l * NE + e) * 1024 * 256 : p.ws1 + (size_t)l * 1024 * 256);
;         const int hc0 = hb * 32;
;         c.src = W + hc0 + (lane & 7) * 4; c.ld = 256; c.dst = p.w13t + (size_t)e * 512 * 1024; c.K = 1024;
;         c.r0 = (hc0 >> 7) * 256 + ((hc0 >> 5) & 3) * 32 + mat * 16; c.k0 = ks * 32; c.perm = 0;
;     } else {
;         s -= NS_W13;
;         const int e = s >> 8, r = s & 255, nb = r & 31, ks = r >> 5;
;         const float* W2 = e < NE ? p.w2 + ((size_t)l * NE + e) * 256 * 1024 : p.ws2 + (size_t)l * 256 * 1024;
;         c.src = W2 + nb * 32 + (lane & 7) * 4; c.ld = 1024; c.dst = p.w2t + (size_t)e * 1024 * 256; c.K = 256; c.r0 = (nb >> 3) * 256 + ((nb & 7) >> 1) * 32 + (nb & 1) * 8; c.k0 = ks * 32; c.perm = 1;
;     }
;     return c;
; }
; DEVI void cv_next(const Params& p, int l, int s, int lane, int stride, CvRun& run) {
;     ...
;     run.c = cv_slice(p, l, s, lane); run.left = 0;
;     if ((stride & 511) == 0) {
;         if (s < NS_W13) { const int e = s >> 9, es = stride >> 9; if (e < NE) { run.left = (NE - 1 - e) / es; run.sstep = (long)es * 1024 * 256; run.dstep = (long)es * 512 * 1024; } }
;         else { const int e = (s - NS_W13) >> 8, es = stride >> 8; if (e < NE) { run.left = (NE - 1 - e) / es; run.sstep = (long)es * 256 * 1024; run.dstep = (long)es * 1024 * 256; } } }
; }
; DEVI void cv_issue(const Params& p, int l, int s, int lane, CvRegs& R, CvRun& run) {
;     R.live = s < NS_SLICES ? 1 : 0;
;     if (R.live) { cv_next(p, l, s, lane, (int)gridDim.x * 8, run); R.c = run.c; const int kq = lane >> 3;
;         const float* sp = R.c.src + (size_t)(R.c.k0 + 2 * kq) * R.c.ld;
;         R.a0 = ld_nt(sp); R.b0 = ld_nt(sp + R.c.ld); R.a1 = ld_nt(sp + (size_t)16 * R.c.ld); R.b1 = ld_nt(sp + (size_t)17 * R.c.ld); }
.LBB0_666:
	s_cmp_lt_i32 s54, 0x30300
	s_mov_b32 s61, s2
	s_cselect_b64 s[14:15], -1, 0
	s_mov_b64 s[98:99], s[14:15]
	s_cmp_gt_i32 s54, 0x302ff
	s_mov_b32 s2, s6
	s_cbranch_scc1 .LBB0_696
	s_cmp_lt_i32 s56, 1
	s_mov_b64 s[16:17], -1
	s_cbranch_scc0 .LBB0_693
	s_cmp_gt_i32 s54, 0x201ff
	s_cselect_b64 s[16:17], -1, 0
	s_mov_b64 s[6:7], -1
	s_and_b64 vcc, exec, s[16:17]
	s_cbranch_vccz .LBB0_670
	s_add_i32 s6, s54, 0xfffdfe00
	s_lshr_b32 s8, s6, 8
	s_and_b32 s10, s54, 0xe0
	s_cmp_lt_u32 s6, 0x10000
	s_cselect_b64 s[6:7], -1, 0
	s_and_b32 s11, s70, 0x3fc0000
	s_and_b64 s[6:7], s[6:7], exec
	s_cselect_b32 s6, 0xc0, s78
	s_cselect_b32 s11, s11, 0
	s_add_u32 s6, s24, s6
	s_addc_u32 s7, s25, 0
	s_load_dwordx2 s[6:7], s[6:7], 0x0
	s_lshl_b32 s11, s11, 2
	s_load_dwordx2 s[20:21], s[24:25], 0x158
	s_waitcnt lgkmcnt(0)
	s_add_u32 s6, s6, s11
	s_addc_u32 s7, s7, 0
	s_and_b32 s11, s71, 0x3e0
	s_lshl_b32 s11, s11, 2
	s_add_u32 s18, s6, s11
	s_addc_u32 s19, s7, 0
	s_lshl_b64 s[6:7], s[8:9], 19
	s_add_u32 s20, s20, s6
	s_addc_u32 s21, s21, s7
	s_and_b32 s6, s71, 0x300
	s_and_b32 s7, s84, 0x60
	s_or_b32 s6, s6, s7
	s_and_b32 s7, s85, 8
	s_or_b32 s8, s6, s7
	s_mov_b64 s[6:7], 0

; #define VM0() asm volatile("s_waitcnt vmcnt(0)" ::: "memory")
; DEVI void attn_unit8(const Params& p, char* smem, int unit, int l, int& cvs  , CvRun& crun) {
;     ...
;         cv_finish(smem + 124928 + wid * 2304, lane, cvr);
;         if (cvr.live) asm volatile("s_waitcnt vmcnt(2)" ::: "memory"); else VM0();
;         __syncthreads();
;         if (T + 2 < NTILE) B_DMA(T + 2, s2);
.Lmy_midlive_a:
	s_waitcnt vmcnt(6)
	s_branch .LBB0_702

; DEVI unsigned cvt_pk_bf16(float lo, float hi) { unsigned r; asm volatile("v_cvt_pk_bf16_f32 %0, %1, %2" : "=v"(r) : "v"(lo), "v"(hi)); return r; }
; DEVI void cv_finish(char* img  , int lane, const CvRegs& R) {
;     if (!R.live) return;
;     const int n4 = (lane & 7) * 4, kq = lane >> 3;
;     const float sc = R.c.perm ? 16.f : 1.f;
; #pragma unroll
;     for (int c = 0; c < 4; ++c) { *(unsigned*)(img + (n4 + c) * 68 + (2 * kq) * 2) = cvt_pk_bf16(R.a0[c] * sc, R.b0[c] * sc); *(unsigned*)(img + (n4 + c) * 68 + (2 * kq + 16) * 2) = cvt_pk_bf16(R.a1[c] * sc, R.b1[c] * sc); }
;     asm volatile("" ::: "memory"); __builtin_amdgcn_wave_barrier();
;     const int n = lane >> 1, half = lane & 1; u32x4 w0, w1;
; #pragma unroll
;     for (int j = 0; j < 4; ++j) { w0[j] = *(const unsigned*)(img + n * 68 + half * 32 + j * 4); w1[j] = *(const unsigned*)(img + n * 68 + half * 32 + 16 + j * 4); }
;     const int row = R.c.perm ? R.c.r0 + 128 * ((n >> 3) & 1) + 16 * ((n >> 2) & 1) + 4 * (n >> 4) + (n & 3) : R.c.r0 + 128 * ((n >> 2) & 1) + 4 * (n >> 3) + (n & 3);
;     bf16_t* d = R.c.dst + (size_t)row * R.c.K + R.c.k0 + half * 16;
;     __builtin_nontemporal_store(w0, (u32x4*)d); __builtin_nontemporal_store(w1, (u32x4*)(d + 8));
;     asm volatile("" ::: "memory"); __builtin_amdgcn_wave_barrier();
; }
.Lmy_cvfin_a:
	s_andn2_b64 vcc, exec, s[98:99]
	s_cbranch_vccnz .LBB0_716
	s_cmp_eq_u32 s95, 0
	s_cselect_b64 vcc, -1, 0
	v_cndmask_b32_e64 v82, v181, 1.0, vcc
	s_waitcnt vmcnt(5)
	v_mul_f32_e32 v83, v82, v154
	v_mul_f32_e32 v84, v82, v158
	v_cvt_pk_bf16_f32 v83, v83, v84
	v_add_u32_e32 v84, v200, v201
	ds_write_b32 v84, v83
	v_mul_f32_e32 v83, v82, v162
	v_mul_f32_e32 v85, v82, v166
	v_cvt_pk_bf16_f32 v83, v83, v85
	ds_write_b32 v84, v83 offset:32
	v_mul_f32_e32 v83, v82, v155
	v_mul_f32_e32 v85, v82, v159
	v_cvt_pk_bf16_f32 v83, v83, v85
	ds_write_b32 v84, v83 offset:68
	v_mul_f32_e32 v83, v82, v163
	v_mul_f32_e32 v85, v82, v167
	v_cvt_pk_bf16_f32 v83, v83, v85
	ds_write_b32 v84, v83 offset:100
	v_mul_f32_e32 v83, v82, v156
	v_mul_f32_e32 v85, v82, v160
	v_cvt_pk_bf16_f32 v83, v83, v85
	ds_write_b32 v84, v83 offset:136
	v_mul_f32_e32 v83, v82, v164
	v_mul_f32_e32 v85, v82, v168
	v_cvt_pk_bf16_f32 v83, v83, v85
	ds_write_b32 v84, v83 offset:168
	v_mul_f32_e32 v83, v82, v157
	v_mul_f32_e32 v85, v82, v161
	v_cvt_pk_bf16_f32 v83, v83, v85
	ds_write_b32 v84, v83 offset:204
	v_mul_f32_e32 v83, v82, v165
	v_mul_f32_e32 v82, v82, v169
	v_cndmask_b32_e32 v90, v196, v197, vcc
	v_cvt_pk_bf16_f32 v82, v83, v82
	ds_write_b32 v84, v82 offset:236
	v_add_u32_e32 v84, v198, v199
	v_or_b32_e32 v90, v90, v195
	ds_read2_b32 v[82:83], v84 offset1:1
	ds_read2_b32 v[86:87], v84 offset0:4 offset1:5
	ds_read2_b32 v[88:89], v84 offset0:6 offset1:7
	ds_read2_b32 v[84:85], v84 offset0:2 offset1:3
	v_add_u32_e32 v90, s8, v90
	v_mad_i64_i32 v[90:91], s[6:7], v90, s94, 0
	v_lshl_add_u64 v[90:91], v[90:91], 1, v[182:183]
	s_ashr_i32 s11, s10, 31
	v_lshl_add_u64 v[90:91], s[10:11], 1, v[90:91]
	v_lshlrev_b32_e32 v174, 1, v180
	v_lshl_add_u64 v[90:91], v[90:91], 0, v[174:175]
	s_waitcnt lgkmcnt(0)
	global_store_dwordx4 v[90:91], v[82:85], off nt
	global_store_dwordx4 v[90:91], v[86:89], off offset:16 nt

; DEVI f32x4 ld_nt(const float* p) { return __builtin_nontemporal_load((const f32x4*)p); }
; DEVI CvSlice cv_slice(const Params& p, int l, int s, int lane) {
;     CvSlice c;
;     if (s < NS_W13) {
;         const int e = s >> 9, r = s & 511, hb = r & 7, mat = (r >> 3) & 1, ks = r >> 4;
;         const float* W = mat ? (e < NE ? p.w3 + ((size_t)l * NE + e) * 1024 * 256 : p.ws3 + (size_t)l * 1024 * 256)
;                              : (e < NE ? p.w1 + ((size_t)l * NE + e) * 1024 * 256 : p.ws1 + (size_t)l * 1024 * 256);
;         const int hc0 = hb * 32;
;         c.src = W + hc0 + (lane & 7) * 4; c.ld = 256; c.dst = p.w13t + (size_t)e * 512 * 1024; c.K = 1024;
;         c.r0 = (hc0 >> 7) * 256 + ((hc0 >> 5) & 3) * 32 + mat * 16; c.k0 = ks * 32; c.perm = 0;
;     } else {
;         s -= NS_W13;
;         const int e = s >> 8, r = s & 255, nb = r & 31, ks = r >> 5;
;         const float* W2 = e < NE ? p.w2 + ((size_t)l * NE + e) * 256 * 1024 : p.ws2 + (size_t)l * 256 * 1024;
;         c.src = W2 + nb * 32 + (lane & 7) * 4; c.ld = 1024; c.dst = p.w2t + (size_t)e * 1024 * 256; c.K = 256; c.r0 = (nb >> 3) * 256 + ((nb & 7) >> 1) * 32 + (nb & 1) * 8; c.k0 = ks * 32; c.perm = 1;
;     }
;     return c;
; }
; DEVI void cv_next(const Params& p, int l, int s, int lane, int stride, CvRun& run) {
;     ...
;     run.c = cv_slice(p, l, s, lane); run.left = 0;
;     if ((stride & 511) == 0) {
;         if (s < NS_W13) { const int e = s >> 9, es = stride >> 9; if (e < NE) { run.left = (NE - 1 - e) / es; run.sstep = (long)es * 1024 * 256; run.dstep = (long)es * 512 * 1024; } }
;         else { const int e = (s - NS_W13) >> 8, es = stride >> 8; if (e < NE) { run.left = (NE - 1 - e) / es; run.sstep = (long)es * 256 * 1024; run.dstep = (long)es * 1024 * 256; } } }
; }
; DEVI void cv_issue(const Params& p, int l, int s, int lane, CvRegs& R, CvRun& run) {
;     R.live = s < NS_SLICES ? 1 : 0;
;     if (R.live) { cv_next(p, l, s, lane, (int)gridDim.x * 8, run); R.c = run.c; const int kq = lane >> 3;
;         const float* sp = R.c.src + (size_t)(R.c.k0 + 2 * kq) * R.c.ld;
;         R.a0 = ld_nt(sp); R.b0 = ld_nt(sp + R.c.ld); R.a1 = ld_nt(sp + (size_t)16 * R.c.ld); R.b1 = ld_nt(sp + (size_t)17 * R.c.ld); }
.LBB0_2230:
	s_cmp_lt_i32 s54, 0x30300
	s_mov_b32 s2, s61
	s_cselect_b64 s[14:15], -1, 0
	s_mov_b64 s[98:99], s[14:15]
	s_cmp_gt_i32 s54, 0x302ff
	s_mov_b32 s61, s6
	s_cbranch_scc1 .LBB0_2260
	s_cmp_lt_i32 s56, 1
	s_mov_b64 s[16:17], -1
	s_cbranch_scc0 .LBB0_2257
	s_cmp_gt_i32 s54, 0x201ff
	s_cselect_b64 s[16:17], -1, 0
	s_mov_b64 s[6:7], -1
	s_and_b64 vcc, exec, s[16:17]
	s_cbranch_vccz .LBB0_2234
	s_add_i32 s6, s54, 0xfffdfe00
	s_lshr_b32 s8, s6, 8
	s_and_b32 s10, s54, 0xe0
	s_cmp_lt_u32 s6, 0x10000
	s_cselect_b64 s[6:7], -1, 0
	s_and_b32 s11, s89, 0x3fc0000
	s_bitset1_b32 s11, 26
	s_and_b64 s[6:7], s[6:7], exec
	s_cselect_b32 s6, 0xc0, s79
	s_cselect_b32 s11, s11, 0x40000
	s_add_u32 s6, s24, s6
	s_addc_u32 s7, s25, 0
	s_load_dwordx2 s[6:7], s[6:7], 0x0
	s_lshl_b32 s11, s11, 2
	s_load_dwordx2 s[20:21], s[24:25], 0x158
	s_waitcnt lgkmcnt(0)
	s_add_u32 s6, s6, s11
	s_addc_u32 s7, s7, 0
	s_and_b32 s11, s84, 0x3e0
	s_lshl_b32 s11, s11, 2
	s_add_u32 s18, s6, s11
	s_addc_u32 s19, s7, 0
	s_lshl_b64 s[6:7], s[8:9], 19
	s_add_u32 s20, s20, s6
	s_addc_u32 s21, s21, s7
	s_and_b32 s6, s84, 0x300
	s_and_b32 s7, s85, 0x60
	s_or_b32 s6, s6, s7
	s_and_b32 s7, s88, 8
	s_or_b32 s8, s6, s7
	s_mov_b64 s[6:7], 0

; DEVI unsigned cvt_pk_bf16(float lo, float hi) { unsigned r; asm volatile("v_cvt_pk_bf16_f32 %0, %1, %2" : "=v"(r) : "v"(lo), "v"(hi)); return r; }
; DEVI void cv_finish(char* img  , int lane, const CvRegs& R) {
;     if (!R.live) return;
;     const int n4 = (lane & 7) * 4, kq = lane >> 3;
;     const float sc = R.c.perm ? 16.f : 1.f;
; #pragma unroll
;     for (int c = 0; c < 4; ++c) { *(unsigned*)(img + (n4 + c) * 68 + (2 * kq) * 2) = cvt_pk_bf16(R.a0[c] * sc, R.b0[c] * sc); *(unsigned*)(img + (n4 + c) * 68 + (2 * kq + 16) * 2) = cvt_pk_bf16(R.a1[c] * sc, R.b1[c] * sc); }
;     asm volatile("" ::: "memory"); __builtin_amdgcn_wave_barrier();
;     const int n = lane >> 1, half = lane & 1; u32x4 w0, w1;
; #pragma unroll
;     for (int j = 0; j < 4; ++j) { w0[j] = *(const unsigned*)(img + n * 68 + half * 32 + j * 4); w1[j] = *(const unsigned*)(img + n * 68 + half * 32 + 16 + j * 4); }
;     const int row = R.c.perm ? R.c.r0 + 128 * ((n >> 3) & 1) + 16 * ((n >> 2) & 1) + 4 * (n >> 4) + (n & 3) : R.c.r0 + 128 * ((n >> 2) & 1) + 4 * (n >> 3) + (n & 3);
;     bf16_t* d = R.c.dst + (size_t)row * R.c.K + R.c.k0 + half * 16;
;     __builtin_nontemporal_store(w0, (u32x4*)d); __builtin_nontemporal_store(w1, (u32x4*)(d + 8));
;     asm volatile("" ::: "memory"); __builtin_amdgcn_wave_barrier();
; }
.Lmy_cvfin_b:
	s_andn2_b64 vcc, exec, s[98:99]
	s_cbranch_vccnz .LBB0_2280
	s_cmp_eq_u32 s95, 0
	s_cselect_b64 vcc, -1, 0
	v_cndmask_b32_e64 v82, v186, 1.0, vcc
	s_waitcnt vmcnt(5)
	v_mul_f32_e32 v83, v82, v154
	v_mul_f32_e32 v84, v82, v158
	v_cvt_pk_bf16_f32 v83, v83, v84
	v_add_u32_e32 v84, v201, v202
	ds_write_b32 v84, v83
	v_mul_f32_e32 v83, v82, v162
	v_mul_f32_e32 v85, v82, v166
	v_cvt_pk_bf16_f32 v83, v83, v85
	ds_write_b32 v84, v83 offset:32
	v_mul_f32_e32 v83, v82, v155
	v_mul_f32_e32 v85, v82, v159
	v_cvt_pk_bf16_f32 v83, v83, v85
	ds_write_b32 v84, v83 offset:68
	v_mul_f32_e32 v83, v82, v163
	v_mul_f32_e32 v85, v82, v167
	v_cvt_pk_bf16_f32 v83, v83, v85
	ds_write_b32 v84, v83 offset:100
	v_mul_f32_e32 v83, v82, v156
	v_mul_f32_e32 v85, v82, v160
	v_cvt_pk_bf16_f32 v83, v83, v85
	ds_write_b32 v84, v83 offset:136
	v_mul_f32_e32 v83, v82, v164
	v_mul_f32_e32 v85, v82, v168
	v_cvt_pk_bf16_f32 v83, v83, v85
	ds_write_b32 v84, v83 offset:168
	v_mul_f32_e32 v83, v82, v157
	v_mul_f32_e32 v85, v82, v161
	v_cvt_pk_bf16_f32 v83, v83, v85
	ds_write_b32 v84, v83 offset:204
	v_mul_f32_e32 v83, v82, v165
	v_mul_f32_e32 v82, v82, v169
	v_cndmask_b32_e32 v90, v197, v198, vcc
	v_cvt_pk_bf16_f32 v82, v83, v82
	ds_write_b32 v84, v82 offset:236
	v_add_u32_e32 v84, v199, v200
	v_or_b32_e32 v90, v90, v196
	ds_read2_b32 v[82:83], v84 offset1:1
	ds_read2_b32 v[86:87], v84 offset0:4 offset1:5
	ds_read2_b32 v[88:89], v84 offset0:6 offset1:7
	ds_read2_b32 v[84:85], v84 offset0:2 offset1:3
	v_add_u32_e32 v90, s8, v90
	v_mad_i64_i32 v[90:91], s[6:7], v90, s94, 0
	v_lshl_add_u64 v[90:91], v[90:91], 1, v[182:183]
	s_ashr_i32 s11, s10, 31
	v_lshl_add_u64 v[90:91], s[10:11], 1, v[90:91]
	v_lshlrev_b32_e32 v174, 1, v180
	v_lshl_add_u64 v[90:91], v[90:91], 0, v[174:175]
	s_waitcnt lgkmcnt(0)
	global_store_dwordx4 v[90:91], v[82:85], off nt
	global_store_dwordx4 v[90:91], v[86:89], off offset:16 nt

; #define LAS __attribute__((address_space(3)))
; #define PHASE(PH, L) do { run_phase<PH>(fresh_params(), smem, L); } while (0)
; #define GRID_BARRIER() do { XcdBarrier b_; b_.bar = fresh_params().bar; b_.x = xb_xcc_id(); b_.st = (volatile LAS unsigned*)(LAS char*)(smem + LDS_BYTES - 16); xcd_barrier(b_); } while (0)
; #define LAYER(l, LAST) do { PHASE_B(2, l); PHASE_B(3, l); PHASE_B(4, l); PHASE_B(5, l); PHASE_B(6, l); PHASE_B(7, l); PHASE_B(8, l); PHASE_B(9, l); PHASE(15, l); GRID_BARRIER(); PHASE_B(11, l); PHASE_B(12, l); \
;         PHASE(13, l); if (!(LAST)) GRID_BARRIER(); \
;         if (DUP_MASK & (1 << 13)) { GRID_BARRIER(); PHASE(13, l); GRID_BARRIER(); } } while (0)
; __global__ void __launch_bounds__(512, 2) k_mega(Params p_unused) {
;     extern __shared__ __attribute__((aligned(16))) char smem[];
;     { volatile LAS unsigned* xbw = (volatile LAS unsigned*)(LAS char*)(smem + LDS_BYTES - 16);
;       if (threadIdx.x == 0) { xbw[0] = 0u; xbw[1] = 0u; xbw[2] = 0u; xbw[3] = 0u; }
;       __syncthreads();
;       (void)xcd_barrier_post(fresh_params().bar, xbw); }
;     PHASE(0, 0); GRID_BARRIER(); if (DUP_MASK & 1) { PHASE(0, 0); GRID_BARRIER(); }
;     PHASE(1, 0); GRID_BARRIER(); if (DUP_MASK & 2) { PHASE(1, 0); GRID_BARRIER(); }
;     ...
;     LAYER(0, false);
;     LAYER(1, true);
; }
	.amdhsa_kernel _Z6k_mega6Params
		.amdhsa_group_segment_fixed_size 0
		.amdhsa_private_segment_fixed_size 0
		.amdhsa_kernarg_size 816
		.amdhsa_user_sgpr_count 2
		.amdhsa_user_sgpr_dispatch_ptr 0
		.amdhsa_user_sgpr_queue_ptr 0
		.amdhsa_user_sgpr_kernarg_segment_ptr 1
		.amdhsa_user_sgpr_dispatch_id 0
		.amdhsa_user_sgpr_kernarg_preload_length 0
		.amdhsa_user_sgpr_kernarg_preload_offset 0
		.amdhsa_user_sgpr_private_segment_size 0
		.amdhsa_uses_dynamic_stack 0
		.amdhsa_enable_private_segment 0
		.amdhsa_system_sgpr_workgroup_id_x 1
		.amdhsa_system_sgpr_workgroup_id_y 0
		.amdhsa_system_sgpr_workgroup_id_z 0
		.amdhsa_system_sgpr_workgroup_info 0
		.amdhsa_system_vgpr_workitem_id 0
		.amdhsa_next_free_vgpr 249
		.amdhsa_next_free_sgpr 100
		.amdhsa_accum_offset 252
		.amdhsa_reserve_vcc 1
		.amdhsa_float_round_mode_32 0
		.amdhsa_float_round_mode_16_64 0
		.amdhsa_float_denorm_mode_32 3
		.amdhsa_float_denorm_mode_16_64 3
		.amdhsa_dx10_clamp 1
		.amdhsa_ieee_mode 1
		.amdhsa_fp16_overflow 0
		.amdhsa_tg_split 0
		.amdhsa_exception_fp_ieee_invalid_op 0
		.amdhsa_exception_fp_denorm_src 0
		.amdhsa_exception_fp_ieee_div_zero 0
		.amdhsa_exception_fp_ieee_overflow 0
		.amdhsa_exception_fp_ieee_underflow 0
		.amdhsa_exception_fp_ieee_inexact 0
		.amdhsa_exception_int_div_zero 0
	.end_amdhsa_kernel

; #define LAS __attribute__((address_space(3)))
; #define PHASE(PH, L) do { run_phase<PH>(fresh_params(), smem, L); } while (0)
; #define GRID_BARRIER() do { XcdBarrier b_; b_.bar = fresh_params().bar; b_.x = xb_xcc_id(); b_.st = (volatile LAS unsigned*)(LAS char*)(smem + LDS_BYTES - 16); xcd_barrier(b_); } while (0)
; #define LAYER(l, LAST) do { PHASE_B(2, l); PHASE_B(3, l); PHASE_B(4, l); PHASE_B(5, l); PHASE_B(6, l); PHASE_B(7, l); PHASE_B(8, l); PHASE_B(9, l); PHASE(15, l); GRID_BARRIER(); PHASE_B(11, l); PHASE_B(12, l); \
;         PHASE(13, l); if (!(LAST)) GRID_BARRIER(); \
;         if (DUP_MASK & (1 << 13)) { GRID_BARRIER(); PHASE(13, l); GRID_BARRIER(); } } while (0)
; __global__ void __launch_bounds__(512, 2) k_mega(Params p_unused) {
;     extern __shared__ __attribute__((aligned(16))) char smem[];
;     { volatile LAS unsigned* xbw = (volatile LAS unsigned*)(LAS char*)(smem + LDS_BYTES - 16);
;       if (threadIdx.x == 0) { xbw[0] = 0u; xbw[1] = 0u; xbw[2] = 0u; xbw[3] = 0u; }
;       __syncthreads();
;       (void)xcd_barrier_post(fresh_params().bar, xbw); }
;     PHASE(0, 0); GRID_BARRIER(); if (DUP_MASK & 1) { PHASE(0, 0); GRID_BARRIER(); }
;     PHASE(1, 0); GRID_BARRIER(); if (DUP_MASK & 2) { PHASE(1, 0); GRID_BARRIER(); }
;     ...
;     LAYER(0, false);
;     LAYER(1, true);
; }
.Lfunc_end0:
	.size	_Z6k_mega6Params, .Lfunc_end0-_Z6k_mega6Params
	.set _Z6k_mega6Params.num_vgpr, 249
	.set _Z6k_mega6Params.num_agpr, 0
	.set _Z6k_mega6Params.numbered_sgpr, 100
	.set _Z6k_mega6Params.num_named_barrier, 0
	.set _Z6k_mega6Params.private_seg_size, 0
	.set _Z6k_mega6Params.uses_vcc, 1
	.set _Z6k_mega6Params.uses_flat_scratch, 0
	.set _Z6k_mega6Params.has_dyn_sized_stack, 0
	.set _Z6k_mega6Params.has_recursion, 0
	.set _Z6k_mega6Params.has_indirect_call, 0

; #define LAS __attribute__((address_space(3)))
; #define PHASE(PH, L) do { run_phase<PH>(fresh_params(), smem, L); } while (0)
; #define GRID_BARRIER() do { XcdBarrier b_; b_.bar = fresh_params().bar; b_.x = xb_xcc_id(); b_.st = (volatile LAS unsigned*)(LAS char*)(smem + LDS_BYTES - 16); xcd_barrier(b_); } while (0)
; #define LAYER(l, LAST) do { PHASE_B(2, l); PHASE_B(3, l); PHASE_B(4, l); PHASE_B(5, l); PHASE_B(6, l); PHASE_B(7, l); PHASE_B(8, l); PHASE_B(9, l); PHASE(15, l); GRID_BARRIER(); PHASE_B(11, l); PHASE_B(12, l); \
;         PHASE(13, l); if (!(LAST)) GRID_BARRIER(); \
;         if (DUP_MASK & (1 << 13)) { GRID_BARRIER(); PHASE(13, l); GRID_BARRIER(); } } while (0)
; __global__ void __launch_bounds__(512, 2) k_mega(Params p_unused) {
;     extern __shared__ __attribute__((aligned(16))) char smem[];
;     { volatile LAS unsigned* xbw = (volatile LAS unsigned*)(LAS char*)(smem + LDS_BYTES - 16);
;       if (threadIdx.x == 0) { xbw[0] = 0u; xbw[1] = 0u; xbw[2] = 0u; xbw[3] = 0u; }
;       __syncthreads();
;       (void)xcd_barrier_post(fresh_params().bar, xbw); }
;     PHASE(0, 0); GRID_BARRIER(); if (DUP_MASK & 1) { PHASE(0, 0); GRID_BARRIER(); }
;     PHASE(1, 0); GRID_BARRIER(); if (DUP_MASK & 2) { PHASE(1, 0); GRID_BARRIER(); }
;     ...
;     LAYER(0, false);
;     LAYER(1, true);
; }
amdhsa.kernels:
  - .agpr_count:     0
    .args:
      - .offset:         0
        .size:           560
        .value_kind:     by_value
      - .offset:         560
        .size:           4
        .value_kind:     hidden_block_count_x
      - .offset:         564
        .size:           4
        .value_kind:     hidden_block_count_y
      - .offset:         568
        .size:           4
        .value_kind:     hidden_block_count_z
      - .offset:         572
        .size:           2
        .value_kind:     hidden_group_size_x
      - .offset:         574
        .size:           2
        .value_kind:     hidden_group_size_y
      - .offset:         576
        .size:           2
        .value_kind:     hidden_group_size_z
      - .offset:         578
        .size:           2
        .value_kind:     hidden_remainder_x
      - .offset:         580
        .size:           2
        .value_kind:     hidden_remainder_y
      - .offset:         582
        .size:           2
        .value_kind:     hidden_remainder_z
      - .offset:         600
        .size:           8
        .value_kind:     hidden_global_offset_x
      - .offset:         608
        .size:           8
        .value_kind:     hidden_global_offset_y
      - .offset:         616
        .size:           8
        .value_kind:     hidden_global_offset_z
      - .offset:         624
        .size:           2
        .value_kind:     hidden_grid_dims
      - .offset:         680
        .size:           4
        .value_kind:     hidden_dynamic_lds_size
    .group_segment_fixed_size: 0
    .kernarg_segment_align: 8
    .kernarg_segment_size: 816
    .language:       OpenCL C
    .language_version:
      - 2
      - 0
    .max_flat_workgroup_size: 512
    .name:           _Z6k_mega6Params
    .private_segment_fixed_size: 0
    .sgpr_count:     106
    .sgpr_spill_count: 9
    .symbol:         _Z6k_mega6Params.kd
    .uniform_work_group_size: 1
    .uses_dynamic_stack: false
    .vgpr_count:     249
    .vgpr_spill_count: 0
    .wavefront_size: 64
